# attention<0> epilogue: O tile transposed through free LDS above the mask table, 16 scattered dwordx2 stores -> 8 coalesced dwordx4 stores
# speedup vs baseline: 1.0303x; 1.0034x over previous
.LBB0_1251:
	v_bfe_u32 v203, v219, 4, 2
	v_lshrrev_b32_e32 v202, 6, v219
	v_mul_u32_u24_e32 v202, 0x1400, v202
	v_mul_u32_u24_e32 v194, 0x110, v166
	v_add_u32_e32 v202, 0x18000, v202
	v_mul_u32_u24_e32 v195, 0x110, v203
	v_lshl_add_u32 v194, v203, 3, v194
	v_lshl_add_u32 v195, v166, 4, v195
	v_add_u32_e32 v194, v202, v194
	v_add_u32_e32 v195, v202, v195
	v_sub_u32_e32 v202, v203, v166
	v_lshlrev_b32_e32 v203, 3, v203
	v_lshlrev_b32_e32 v202, 12, v202
	v_lshl_add_u32 v202, v166, 4, v202
	s_mov_b64 s[60:61], 0x4000
	v_sub_u32_e32 v202, v202, v203
	v_ashrrev_i32_e32 v203, 31, v202
	s_xor_b64 s[18:19], s[16:17], -1
	v_div_scale_f32 v70, s[16:17], v103, v103, 1.0
	v_rcp_f32_e32 v71, v70
	v_div_scale_f32 v72, vcc, 1.0, v103, 1.0
	v_ashrrev_i32_e32 v215, 31, v214
	v_fma_f32 v73, -v70, v71, 1.0
	v_fmac_f32_e32 v71, v73, v71
	v_mul_f32_e32 v73, v72, v71
	v_fma_f32 v74, -v70, v73, v72
	v_fmac_f32_e32 v73, v74, v71
	v_fma_f32 v70, -v70, v73, v72
	v_div_fmas_f32 v70, v70, v71, v73
	v_div_fixup_f32 v70, v70, v103, 1.0
	v_lshlrev_b64 v[72:73], 12, v[214:215]
	v_pk_mul_f32 v[44:45], v[70:71], v[44:45] op_sel_hi:[0,1]
	v_pk_mul_f32 v[42:43], v[70:71], v[42:43] op_sel_hi:[0,1]
	v_lshl_add_u64 v[72:73], v[192:193], 0, v[72:73]
	v_cvt_pk_bf16_f32 v42, v42, v43
	v_cvt_pk_bf16_f32 v43, v44, v45
	ds_write_b64 v194, v[42:43] offset:192
	v_div_scale_f32 v42, s[16:17], v102, v102, 1.0
	v_rcp_f32_e32 v43, v42
	v_pk_mul_f32 v[40:41], v[70:71], v[40:41] op_sel_hi:[0,1]
	v_pk_mul_f32 v[38:39], v[70:71], v[38:39] op_sel_hi:[0,1]
	v_cvt_pk_bf16_f32 v38, v38, v39
	v_cvt_pk_bf16_f32 v39, v40, v41
	ds_write_b64 v194, v[38:39] offset:224
	v_fma_f32 v38, -v42, v43, 1.0
	v_fmac_f32_e32 v43, v38, v43
	v_div_scale_f32 v38, vcc, 1.0, v102, 1.0
	v_mul_f32_e32 v39, v38, v43
	v_fma_f32 v40, -v42, v39, v38
	v_fmac_f32_e32 v39, v40, v43
	v_fma_f32 v38, -v42, v39, v38
	v_div_fmas_f32 v38, v38, v43, v39
	v_ashrrev_i32_e32 v213, 31, v212
	v_div_fixup_f32 v38, v38, v102, 1.0
	v_pk_mul_f32 v[68:69], v[68:69], v[70:71] op_sel_hi:[1,0]
	v_pk_mul_f32 v[66:67], v[66:67], v[70:71] op_sel_hi:[1,0]
	v_pk_mul_f32 v[64:65], v[70:71], v[64:65] op_sel_hi:[0,1]
	v_pk_mul_f32 v[62:63], v[70:71], v[62:63] op_sel_hi:[0,1]
	v_pk_mul_f32 v[60:61], v[70:71], v[60:61] op_sel_hi:[0,1]
	v_pk_mul_f32 v[58:59], v[70:71], v[58:59] op_sel_hi:[0,1]
	v_pk_mul_f32 v[56:57], v[70:71], v[56:57] op_sel_hi:[0,1]
	v_pk_mul_f32 v[54:55], v[70:71], v[54:55] op_sel_hi:[0,1]
	v_pk_mul_f32 v[52:53], v[70:71], v[52:53] op_sel_hi:[0,1]
	v_pk_mul_f32 v[50:51], v[70:71], v[50:51] op_sel_hi:[0,1]
	v_pk_mul_f32 v[48:49], v[70:71], v[48:49] op_sel_hi:[0,1]
	v_pk_mul_f32 v[46:47], v[70:71], v[46:47] op_sel_hi:[0,1]
	v_lshlrev_b64 v[40:41], 12, v[212:213]
	v_pk_mul_f32 v[30:31], v[38:39], v[30:31] op_sel_hi:[0,1]
	v_pk_mul_f32 v[28:29], v[38:39], v[28:29] op_sel_hi:[0,1]
	v_pk_mul_f32 v[26:27], v[38:39], v[26:27] op_sel_hi:[0,1]
	v_pk_mul_f32 v[24:25], v[38:39], v[24:25] op_sel_hi:[0,1]
	v_pk_mul_f32 v[22:23], v[38:39], v[22:23] op_sel_hi:[0,1]
	v_pk_mul_f32 v[20:21], v[38:39], v[20:21] op_sel_hi:[0,1]
	v_pk_mul_f32 v[18:19], v[38:39], v[18:19] op_sel_hi:[0,1]
	v_pk_mul_f32 v[16:17], v[38:39], v[16:17] op_sel_hi:[0,1]
	v_pk_mul_f32 v[14:15], v[38:39], v[14:15] op_sel_hi:[0,1]
	v_pk_mul_f32 v[12:13], v[38:39], v[12:13] op_sel_hi:[0,1]
	v_pk_mul_f32 v[10:11], v[38:39], v[10:11] op_sel_hi:[0,1]
	v_pk_mul_f32 v[8:9], v[38:39], v[8:9] op_sel_hi:[0,1]
	v_pk_mul_f32 v[6:7], v[38:39], v[6:7] op_sel_hi:[0,1]
	v_pk_mul_f32 v[4:5], v[38:39], v[4:5] op_sel_hi:[0,1]
	v_pk_mul_f32 v[2:3], v[38:39], v[2:3] op_sel_hi:[0,1]
	v_pk_mul_f32 v[0:1], v[38:39], v[0:1] op_sel_hi:[0,1]
	v_cvt_pk_bf16_f32 v66, v66, v67
	v_cvt_pk_bf16_f32 v67, v68, v69
	v_cvt_pk_bf16_f32 v62, v62, v63
	v_cvt_pk_bf16_f32 v63, v64, v65
	v_cvt_pk_bf16_f32 v58, v58, v59
	v_cvt_pk_bf16_f32 v59, v60, v61
	v_cvt_pk_bf16_f32 v54, v54, v55
	v_cvt_pk_bf16_f32 v55, v56, v57
	v_cvt_pk_bf16_f32 v50, v50, v51
	v_cvt_pk_bf16_f32 v51, v52, v53
	v_cvt_pk_bf16_f32 v46, v46, v47
	v_cvt_pk_bf16_f32 v47, v48, v49
	v_lshl_add_u64 v[40:41], v[192:193], 0, v[40:41]
	v_cvt_pk_bf16_f32 v28, v28, v29
	v_cvt_pk_bf16_f32 v29, v30, v31
	v_cvt_pk_bf16_f32 v24, v24, v25
	v_cvt_pk_bf16_f32 v25, v26, v27
	v_cvt_pk_bf16_f32 v20, v20, v21
	v_cvt_pk_bf16_f32 v21, v22, v23
	v_cvt_pk_bf16_f32 v16, v16, v17
	v_cvt_pk_bf16_f32 v17, v18, v19
	v_cvt_pk_bf16_f32 v12, v12, v13
	v_cvt_pk_bf16_f32 v13, v14, v15
	v_cvt_pk_bf16_f32 v8, v8, v9
	v_cvt_pk_bf16_f32 v9, v10, v11
	v_cvt_pk_bf16_f32 v4, v4, v5
	v_cvt_pk_bf16_f32 v5, v6, v7
	v_cvt_pk_bf16_f32 v0, v0, v1
	v_cvt_pk_bf16_f32 v1, v2, v3
	s_mov_b64 s[16:17], 0
	s_and_b64 vcc, exec, s[18:19]
	ds_write_b64 v194, v[66:67]
	ds_write_b64 v194, v[62:63] offset:32
	ds_write_b64 v194, v[58:59] offset:64
	ds_write_b64 v194, v[54:55] offset:96
	ds_write_b64 v194, v[50:51] offset:128
	ds_write_b64 v194, v[46:47] offset:160
	ds_read_b128 v[44:47], v195
	ds_read_b128 v[48:51], v195 offset:1088
	ds_read_b128 v[52:55], v195 offset:2176
	ds_read_b128 v[56:59], v195 offset:3264
	ds_write_b64 v194, v[28:29]
	ds_write_b64 v194, v[24:25] offset:32
	ds_write_b64 v194, v[20:21] offset:64
	ds_write_b64 v194, v[16:17] offset:96
	ds_write_b64 v194, v[12:13] offset:128
	ds_write_b64 v194, v[8:9] offset:160
	ds_write_b64 v194, v[4:5] offset:192
	ds_write_b64 v194, v[0:1] offset:224
	ds_read_b128 v[0:3], v195
	ds_read_b128 v[4:7], v195 offset:1088
	ds_read_b128 v[8:11], v195 offset:2176
	ds_read_b128 v[12:15], v195 offset:3264
	v_lshl_add_u64 v[196:197], v[72:73], 0, v[202:203]
	v_lshl_add_u64 v[208:209], v[40:41], 0, v[202:203]
	s_waitcnt lgkmcnt(0)
	global_store_dwordx4 v[196:197], v[44:47], off
	v_lshl_add_u64 v[196:197], v[196:197], 0, s[60:61]
	global_store_dwordx4 v[196:197], v[48:51], off
	v_lshl_add_u64 v[196:197], v[196:197], 0, s[60:61]
	global_store_dwordx4 v[196:197], v[52:55], off
	v_lshl_add_u64 v[196:197], v[196:197], 0, s[60:61]
	global_store_dwordx4 v[196:197], v[56:59], off
	global_store_dwordx4 v[208:209], v[0:3], off
	v_lshl_add_u64 v[208:209], v[208:209], 0, s[60:61]
	global_store_dwordx4 v[208:209], v[4:7], off
	v_lshl_add_u64 v[208:209], v[208:209], 0, s[60:61]
	global_store_dwordx4 v[208:209], v[8:11], off
	v_lshl_add_u64 v[208:209], v[208:209], 0, s[60:61]
	global_store_dwordx4 v[208:209], v[12:15], off
	s_nop 1
	s_cbranch_vccnz .LBB0_1249
